# DSA scoring loop hand-rescheduled (no canonicalize, batched MFMAs, bitop3 ordf), window-loop mov/LUT-address trims, top-8 max chains interleaved
# speedup vs baseline: 1.1540x; 1.0189x over previous
.LBB0_631:
	v_max_u32_dpp v22, v18, v18 quad_perm:[1,0,3,2] row_mask:0xf bank_mask:0xf bound_ctrl:1
	v_max_u32_dpp v23, v19, v19 quad_perm:[1,0,3,2] row_mask:0xf bank_mask:0xf bound_ctrl:1
	v_max_u32_dpp v24, v20, v20 quad_perm:[1,0,3,2] row_mask:0xf bank_mask:0xf bound_ctrl:1
	v_max_u32_dpp v25, v21, v21 quad_perm:[1,0,3,2] row_mask:0xf bank_mask:0xf bound_ctrl:1
	v_max_u32_dpp v22, v22, v22 quad_perm:[2,3,0,1] row_mask:0xf bank_mask:0xf bound_ctrl:1
	v_max_u32_dpp v23, v23, v23 quad_perm:[2,3,0,1] row_mask:0xf bank_mask:0xf bound_ctrl:1
	v_max_u32_dpp v24, v24, v24 quad_perm:[2,3,0,1] row_mask:0xf bank_mask:0xf bound_ctrl:1
	v_max_u32_dpp v25, v25, v25 quad_perm:[2,3,0,1] row_mask:0xf bank_mask:0xf bound_ctrl:1
	v_max_u32_dpp v22, v22, v22 row_half_mirror row_mask:0xf bank_mask:0xf bound_ctrl:1
	v_max_u32_dpp v23, v23, v23 row_half_mirror row_mask:0xf bank_mask:0xf bound_ctrl:1
	v_max_u32_dpp v24, v24, v24 row_half_mirror row_mask:0xf bank_mask:0xf bound_ctrl:1
	v_max_u32_dpp v25, v25, v25 row_half_mirror row_mask:0xf bank_mask:0xf bound_ctrl:1
	v_max_u32_dpp v22, v22, v22 row_mirror row_mask:0xf bank_mask:0xf bound_ctrl:1
	v_max_u32_dpp v23, v23, v23 row_mirror row_mask:0xf bank_mask:0xf bound_ctrl:1
	v_max_u32_dpp v24, v24, v24 row_mirror row_mask:0xf bank_mask:0xf bound_ctrl:1
	v_max_u32_dpp v25, v25, v25 row_mirror row_mask:0xf bank_mask:0xf bound_ctrl:1
	v_mov_b32_e32 v26, v22
	v_mov_b32_e32 v27, v23
	v_mov_b32_e32 v28, v24
	v_mov_b32_e32 v29, v25
	v_permlane16_swap_b32_e32 v22, v26
	v_permlane16_swap_b32_e32 v23, v27
	v_permlane16_swap_b32_e32 v24, v28
	v_permlane16_swap_b32_e32 v25, v29
	v_max_u32_e32 v22, v22, v26
	v_max_u32_e32 v23, v23, v27
	v_max_u32_e32 v24, v24, v28
	v_max_u32_e32 v25, v25, v29
	v_mov_b32_e32 v26, v22
	v_mov_b32_e32 v27, v23
	v_mov_b32_e32 v28, v24
	v_mov_b32_e32 v29, v25
	v_permlane32_swap_b32_e32 v22, v26
	v_permlane32_swap_b32_e32 v23, v27
	v_permlane32_swap_b32_e32 v24, v28
	v_permlane32_swap_b32_e32 v25, v29
	v_max_u32_e32 v22, v22, v26
	v_max_u32_e32 v23, v23, v27
	v_max_u32_e32 v24, v24, v28
	v_max_u32_e32 v25, v25, v29
	s_and_saveexec_b64 s[14:15], s[46:47]
	s_cbranch_execz .LBB0_630
	s_add_i32 s17, s16, s9
	v_bitop3_b32 v26, v22, 63, v22 bitop3:0xc
	v_cmp_ne_u32_e32 vcc, 0, v22
	s_add_i32 s19, s17, 0x12000
	v_mov_b32_e32 v27, s19
	v_cndmask_b32_e32 v26, -1, v26, vcc
	ds_write_b32 v27, v26
	v_bitop3_b32 v26, v23, 63, v23 bitop3:0xc
	v_cmp_ne_u32_e32 vcc, 0, v23
	s_add_i32 s19, s17, 0x12020
	v_mov_b32_e32 v27, s19
	v_cndmask_b32_e32 v26, -1, v26, vcc
	ds_write_b32 v27, v26
	v_bitop3_b32 v26, v24, 63, v24 bitop3:0xc
	v_cmp_ne_u32_e32 vcc, 0, v24
	s_add_i32 s19, s17, 0x12040
	v_mov_b32_e32 v27, s19
	v_cndmask_b32_e32 v26, -1, v26, vcc
	ds_write_b32 v27, v26
	v_bitop3_b32 v26, v25, 63, v25 bitop3:0xc
	v_cmp_ne_u32_e32 vcc, 0, v25
	s_add_i32 s17, s17, 0x12060
	v_mov_b32_e32 v27, s17
	v_cndmask_b32_e32 v26, -1, v26, vcc
	ds_write_b32 v27, v26
	s_branch .LBB0_630
.LBB0_633:
	s_add_i32 s9, s62, 0xfffffe01
	s_and_b32 s9, s9, -16
	s_cmpk_gt_i32 s62, 0x1fe
	s_cselect_b32 s14, s9, 0
	s_sub_i32 s9, s62, s14
	s_cmp_lt_i32 s9, 0
	s_cbranch_scc1 .LBB0_648
	s_ashr_i32 s15, s14, 31
	s_lshl_b64 s[16:17], s[14:15], 7
	v_lshl_add_u64 v[30:31], v[146:147], 0, s[16:17]
	s_waitcnt vmcnt(2)
	v_lshl_add_u64 v[34:35], v[148:149], 0, s[16:17]
	global_load_dwordx4 v[18:21], v[30:31], off offset:3072
	global_load_dwordx4 v[22:25], v[30:31], off offset:2048
	global_load_dwordx4 v[26:29], v[30:31], off offset:1024
	s_nop 0
	global_load_dwordx4 v[30:33], v[30:31], off
	s_nop 0
	global_load_dwordx4 v[50:53], v[34:35], off offset:3072
	global_load_dwordx4 v[70:73], v[34:35], off offset:2048
	global_load_dwordx4 v[74:77], v[34:35], off offset:1024
	global_load_dwordx4 v[78:81], v[34:35], off
	v_add_u32_e32 v34, s18, v137
	v_subrev_u32_e32 v34, s14, v34
	v_lshl_add_u32 v198, v34, 2, v193
	v_add_lshl_u32 v34, v230, s18, 2
	s_lshl_b32 s16, s14, 2
	v_subrev_u32_e32 v34, s16, v34
	v_mov_b32_e32 v212, 0
	s_and_b32 s15, s9, 0xffffffe0
	s_sub_i32 s63, s62, 31
	v_add_u32_e32 v211, v139, v34
	s_mov_b32 s64, 64
	s_add_i32 s96, s36, 0x1fbb4
	s_add_i32 s97, s36, 0x1fb34
	v_mov_b32_e32 v34, 0
	v_mov_b32_e32 v35, v212
	v_mov_b32_e32 v36, v212
	v_mov_b32_e32 v37, v212
	s_waitcnt vmcnt(9)
	v_mov_b32_e32 v46, 0
	v_mov_b32_e32 v47, v212
	v_mov_b32_e32 v48, v212
	v_mov_b32_e32 v49, v212
	s_waitcnt vmcnt(8)
	v_mov_b32_e32 v42, 0
	v_mov_b32_e32 v43, v212
	v_mov_b32_e32 v44, v212
	v_mov_b32_e32 v45, v212
	v_mov_b32_e32 v38, 0
	v_mov_b32_e32 v39, v212
	v_mov_b32_e32 v40, v212
	v_mov_b32_e32 v41, v212
	s_branch .LBB0_637

.LBB0_637:
	s_sub_i32 s65, s64, 64
	s_sub_i32 s66, s64, 32
	s_cmp_lt_i32 s65, s15
	s_cselect_b64 s[16:17], -1, 0
	s_and_b64 s[18:19], s[16:17], exec
	s_cselect_b32 s18, s66, s65
	s_add_i32 s18, s18, s14
	s_ashr_i32 s19, s18, 31
	s_lshl_b64 s[18:19], s[18:19], 7
	v_lshl_add_u64 v[58:59], v[148:149], 0, s[18:19]
	v_lshl_add_u64 v[66:67], v[146:147], 0, s[18:19]
	global_load_dwordx4 v[110:113], v[58:59], off
	global_load_dwordx4 v[106:109], v[58:59], off offset:1024
	global_load_dwordx4 v[102:105], v[58:59], off offset:2048
	global_load_dwordx4 v[98:101], v[58:59], off offset:3072
	global_load_dwordx4 v[54:57], v[66:67], off
	global_load_dwordx4 v[58:61], v[66:67], off offset:1024
	global_load_dwordx4 v[62:65], v[66:67], off offset:2048
	s_nop 0
	global_load_dwordx4 v[66:69], v[66:67], off offset:3072
	s_waitcnt vmcnt(8)
	v_mfma_f32_16x16x32_bf16 v[216:219], v[78:81], v[10:13], 0
	v_mfma_f32_16x16x32_bf16 v[74:77], v[74:77], v[14:17], v[216:219]
	v_add_u32_e32 v80, s96, v198
	v_mfma_f32_16x16x32_bf16 v[70:73], v[70:73], v[10:13], 0
	s_add_i32 s66, s14, s64
	s_sub_i32 s18, s66, 64
	v_mfma_f32_16x16x32_bf16 v[50:53], v[50:53], v[14:17], v[70:73]
	s_cmp_gt_i32 s18, s63
	s_cselect_b64 s[18:19], -1, 0
	s_cmpk_gt_i32 s9, 0x1fc
	ds_read2_b32 v[70:71], v80 offset0:18 offset1:19
	ds_read2_b32 v[72:73], v80 offset0:2 offset1:3
	ds_read2_b32 v[78:79], v80 offset0:16 offset1:17
	ds_read2_b32 v[80:81], v80 offset1:1
	s_cselect_b64 s[68:69], -1, 0
	s_or_b64 s[68:69], s[18:19], s[68:69]
	s_waitcnt lgkmcnt(3)
	v_add_f32_e32 v90, v74, v71
	s_waitcnt lgkmcnt(2)
	v_add_f32_e32 v86, v50, v73
	v_add_f32_e32 v89, v75, v70
	v_add_f32_e32 v85, v51, v72
	s_waitcnt lgkmcnt(1)
	v_add_f32_e32 v88, v76, v79
	s_waitcnt lgkmcnt(0)
	v_add_f32_e32 v82, v52, v81
	v_add_f32_e32 v87, v77, v78
	v_add_f32_e32 v81, v53, v80
	v_exp_f32_e32 v75, v90
	v_exp_f32_e32 v76, v89
	v_exp_f32_e32 v77, v88
	v_exp_f32_e32 v78, v87
	v_exp_f32_e32 v79, v86
	v_exp_f32_e32 v80, v85
	v_exp_f32_e32 v83, v82
	v_exp_f32_e32 v84, v81
	v_add_u32_e32 v214, s9, v192
	s_mov_b64 s[18:19], -1
	s_and_b64 vcc, exec, s[68:69]
	s_cbranch_vccz .LBB0_639
	v_exp_f32_e32 v75, v90
	v_exp_f32_e32 v79, v89
	v_add_u32_e32 v76, -1, v214
	v_cmp_gt_u32_e32 vcc, s88, v214
	v_exp_f32_e32 v87, v87
	v_add_u32_e32 v77, -2, v214
	v_cndmask_b32_e32 v75, 0, v75, vcc
	v_cmp_gt_u32_e32 vcc, s88, v76
	v_exp_f32_e32 v86, v86
	v_add_u32_e32 v78, -3, v214
	v_cndmask_b32_e32 v76, 0, v79, vcc
	v_exp_f32_e32 v79, v88
	v_add_f32_e32 v89, 0, v75
	v_cmp_gt_u32_e32 vcc, s88, v77
	v_exp_f32_e32 v85, v85
	v_add_u32_e32 v50, -16, v214
	v_add_f32_e32 v88, v89, v76
	v_cndmask_b32_e32 v77, 0, v79, vcc
	v_cmp_gt_u32_e32 vcc, s88, v78
	v_exp_f32_e32 v82, v82
	v_subrev_u32_e32 v80, 17, v214
	v_add_f32_e32 v79, v88, v77
	v_cndmask_b32_e32 v78, 0, v87, vcc
	v_cmp_gt_u32_e32 vcc, s88, v50
	v_exp_f32_e32 v81, v81
	v_subrev_u32_e32 v83, 18, v214
	v_add_f32_e32 v87, v79, v78
	v_cndmask_b32_e32 v79, 0, v86, vcc
	v_cmp_gt_u32_e32 vcc, s88, v80
	v_subrev_u32_e32 v84, 19, v214
	v_add_f32_e32 v50, v79, v87
	v_cndmask_b32_e32 v80, 0, v85, vcc
	v_cmp_gt_u32_e32 vcc, s88, v83
	v_add_f32_e32 v50, v80, v50
	s_mov_b64 s[18:19], 0
	v_cndmask_b32_e32 v83, 0, v82, vcc
	v_cmp_gt_u32_e32 vcc, s88, v84
	v_add_f32_e32 v50, v83, v50
	s_nop 0
	v_cndmask_b32_e32 v84, 0, v81, vcc
	v_add_f32_e32 v50, v84, v50
.LBB0_639:
	s_andn2_b64 vcc, exec, s[18:19]
	s_cbranch_vccnz .LBB0_641
	v_add_f32_e32 v50, 0, v75
	v_add_f32_e32 v50, v50, v76
	v_add_f32_e32 v50, v50, v77
	v_add_f32_e32 v50, v50, v78
	v_add_f32_e32 v50, v79, v50
	v_add_f32_e32 v50, v80, v50
	v_add_f32_e32 v50, v83, v50
	v_add_f32_e32 v50, v84, v50
.LBB0_641:
	v_add_u32_e32 v215, v174, v177
	ds_write_b128 v215, v[30:33]
	ds_write_b128 v215, v[26:29] offset:1152
	ds_write_b128 v215, v[22:25] offset:2304
	ds_write_b128 v215, v[18:21] offset:3456
	v_cvt_pk_bf16_f32 v18, v75, v76
	v_cvt_pk_bf16_f32 v19, v77, v78
	v_cvt_pk_bf16_f32 v20, v79, v80
	v_cvt_pk_bf16_f32 v21, v83, v84
	ds_read_b64_tr_b16 v[24:25], v207
	ds_read_b64_tr_b16 v[22:23], v206
	ds_read_b64_tr_b16 v[26:27], v206 offset:32
	ds_read_b64_tr_b16 v[30:31], v206 offset:64
	ds_read_b64_tr_b16 v[70:71], v206 offset:96
	ds_read_b64_tr_b16 v[28:29], v207 offset:32
	ds_read_b64_tr_b16 v[32:33], v207 offset:64
	ds_read_b64_tr_b16 v[72:73], v207 offset:96
	s_waitcnt lgkmcnt(6)
	v_mfma_f32_16x16x32_bf16 v[82:85], v[18:21], v[22:25], v[46:49]
	v_add_f32_e32 v213, v212, v50
	s_mov_b64 s[18:19], -1
	s_waitcnt lgkmcnt(2)
	v_mfma_f32_16x16x32_bf16 v[86:89], v[18:21], v[26:29], v[42:45]
	s_andn2_b64 vcc, exec, s[16:17]
	s_mov_b64 s[16:17], -1
	s_waitcnt lgkmcnt(1)
	v_mfma_f32_16x16x32_bf16 v[94:97], v[18:21], v[30:33], v[38:41]
	s_waitcnt lgkmcnt(0)
	v_mfma_f32_16x16x32_bf16 v[90:93], v[18:21], v[70:73], v[34:37]
	s_cbranch_vccnz .LBB0_636
	s_cmp_gt_i32 s64, s15
	s_cselect_b64 s[16:17], -1, 0
	s_and_b64 s[18:19], s[16:17], exec
	s_cselect_b32 s18, s65, s64
	s_add_i32 s18, s18, s14
	s_ashr_i32 s19, s18, 31
	s_lshl_b64 s[18:19], s[18:19], 7
	v_lshl_add_u64 v[22:23], v[148:149], 0, s[18:19]
	v_lshl_add_u64 v[18:19], v[146:147], 0, s[18:19]
	global_load_dwordx4 v[78:81], v[22:23], off
	global_load_dwordx4 v[74:77], v[22:23], off offset:1024
	global_load_dwordx4 v[70:73], v[22:23], off offset:2048
	global_load_dwordx4 v[50:53], v[22:23], off offset:3072
	global_load_dwordx4 v[30:33], v[18:19], off
	global_load_dwordx4 v[26:29], v[18:19], off offset:1024
	global_load_dwordx4 v[22:25], v[18:19], off offset:2048
	s_nop 0
	global_load_dwordx4 v[18:21], v[18:19], off offset:3072
	s_waitcnt vmcnt(15)
	v_mfma_f32_16x16x32_bf16 v[220:223], v[110:113], v[10:13], 0
	s_waitcnt vmcnt(14)
	v_mfma_f32_16x16x32_bf16 v[34:37], v[106:109], v[14:17], v[220:223]
	v_add_u32_e32 v48, s97, v211
	s_waitcnt vmcnt(13)
	v_mfma_f32_16x16x32_bf16 v[38:41], v[102:105], v[10:13], 0
	ds_read2_b32 v[42:43], v48 offset0:18 offset1:19
	ds_read2_b32 v[44:45], v48 offset0:2 offset1:3
	ds_read2_b32 v[46:47], v48 offset0:16 offset1:17
	ds_read2_b32 v[48:49], v48 offset1:1
	s_waitcnt vmcnt(12)
	v_mfma_f32_16x16x32_bf16 v[38:41], v[98:101], v[14:17], v[38:41]
	s_sub_i32 s18, s66, 32
	s_cmp_gt_i32 s18, s63
	s_waitcnt lgkmcnt(3)
	v_add_f32_e32 v106, v34, v43
	v_add_f32_e32 v105, v35, v42
	s_waitcnt lgkmcnt(1)
	v_add_f32_e32 v104, v36, v47
	s_nop 0
	v_add_f32_e32 v102, v38, v45
	v_add_f32_e32 v101, v39, v44
	s_waitcnt lgkmcnt(0)
	v_add_f32_e32 v99, v40, v49
	v_add_f32_e32 v103, v37, v46
	v_add_f32_e32 v48, v41, v48
	s_cselect_b64 s[18:19], -1, 0
	s_sub_i32 s65, s9, 32
	s_cmpk_gt_i32 s65, 0x1fc
	v_exp_f32_e32 v42, v106
	v_exp_f32_e32 v43, v105
	v_exp_f32_e32 v44, v104
	v_exp_f32_e32 v45, v103
	v_exp_f32_e32 v46, v102
	v_exp_f32_e32 v47, v101
	v_exp_f32_e32 v49, v99
	v_exp_f32_e32 v100, v48
	s_cselect_b64 s[66:67], -1, 0
	s_or_b64 s[66:67], s[18:19], s[66:67]
	s_mov_b64 s[18:19], -1
	s_and_b64 vcc, exec, s[66:67]
	s_cbranch_vccz .LBB0_644
	v_exp_f32_e32 v98, v106
	v_exp_f32_e32 v105, v105
	v_subrev_u32_e32 v42, 32, v214
	v_exp_f32_e32 v104, v104
	v_subrev_u32_e32 v43, 33, v214
	v_cmp_gt_u32_e32 vcc, s88, v42
	v_exp_f32_e32 v103, v103
	v_subrev_u32_e32 v44, 34, v214
	v_cndmask_b32_e32 v42, 0, v98, vcc
	v_cmp_gt_u32_e32 vcc, s88, v43
	v_exp_f32_e32 v102, v102
	v_subrev_u32_e32 v45, 35, v214
	v_add_f32_e32 v98, 0, v42
	v_cndmask_b32_e32 v43, 0, v105, vcc
	v_cmp_gt_u32_e32 vcc, s88, v44
	v_exp_f32_e32 v101, v101
	v_subrev_u32_e32 v46, 48, v214
	v_add_f32_e32 v98, v98, v43
	v_cndmask_b32_e32 v44, 0, v104, vcc
	v_cmp_gt_u32_e32 vcc, s88, v45
	v_exp_f32_e32 v99, v99
	v_subrev_u32_e32 v47, 49, v214
	v_add_f32_e32 v98, v98, v44
	v_cndmask_b32_e32 v45, 0, v103, vcc
	v_cmp_gt_u32_e32 vcc, s88, v46
	v_exp_f32_e32 v48, v48
	v_subrev_u32_e32 v49, 50, v214
	v_add_f32_e32 v98, v98, v45
	v_cndmask_b32_e32 v46, 0, v102, vcc
	v_cmp_gt_u32_e32 vcc, s88, v47
	v_subrev_u32_e32 v100, 51, v214
	v_add_f32_e32 v98, v46, v98
	v_cndmask_b32_e32 v47, 0, v101, vcc
	v_cmp_gt_u32_e32 vcc, s88, v49
	v_add_f32_e32 v98, v47, v98
	s_mov_b64 s[18:19], 0
	v_cndmask_b32_e32 v49, 0, v99, vcc
	v_cmp_gt_u32_e32 vcc, s88, v100
	v_add_f32_e32 v98, v49, v98
	s_nop 0
	v_cndmask_b32_e32 v100, 0, v48, vcc
	v_add_f32_e32 v98, v100, v98
.LBB0_644:
	s_andn2_b64 vcc, exec, s[18:19]
	s_cbranch_vccnz .LBB0_635
	v_add_f32_e32 v98, 0, v42
	v_add_f32_e32 v98, v98, v43
	v_add_f32_e32 v98, v98, v44
	v_add_f32_e32 v98, v98, v45
	v_add_f32_e32 v98, v46, v98
	v_add_f32_e32 v98, v47, v98
	v_add_f32_e32 v98, v49, v98
	v_add_f32_e32 v98, v100, v98
	s_branch .LBB0_635

.LBB0_721:
	s_or_b64 exec, exec, s[0:1]
	s_lshl_b64 s[0:1], s[4:5], 6
	s_cmpk_lt_u32 s6, 0x100
	v_writelane_b32 v254, s0, 48
	s_cselect_b64 s[4:5], -1, 0
	s_and_b64 vcc, exec, s[4:5]
	v_writelane_b32 v254, s1, 49
	s_cbranch_vccnz .LBB0_738
	s_lshr_b32 s7, s6, 4
	v_readlane_b32 s0, v254, 29
	v_readlane_b32 s10, v254, 34
	s_cmp_gt_i32 s0, s7
	v_readlane_b32 s11, v254, 35
	s_cbranch_scc1 .LBB0_725
	s_waitcnt vmcnt(2)
	v_lshlrev_b32_e32 v56, 16, v174
	v_and_b32_e32 v57, 0xffff0000, v174
	s_mov_b32 s0, 0x3eb504f3
	v_pk_mul_f32 v[64:65], v[56:57], s[0:1] op_sel_hi:[1,0]
	v_and_b32_e32 v56, 0xffff0000, v175
	v_lshlrev_b32_e32 v57, 16, v175
	v_pk_mul_f32 v[66:67], v[56:57], s[0:1] op_sel_hi:[1,0]
	v_lshlrev_b32_e32 v56, 16, v172
	v_and_b32_e32 v57, 0xffff0000, v172
	v_pk_mul_f32 v[68:69], v[56:57], s[0:1] op_sel_hi:[1,0]
	v_and_b32_e32 v56, 0xffff0000, v173
	v_lshlrev_b32_e32 v57, 16, v173
	v_pk_mul_f32 v[70:71], v[56:57], s[0:1] op_sel_hi:[1,0]
	v_lshlrev_b32_e32 v56, 16, v170
	v_and_b32_e32 v57, 0xffff0000, v170
	v_pk_mul_f32 v[72:73], v[56:57], s[0:1] op_sel_hi:[1,0]
	v_and_b32_e32 v56, 0xffff0000, v171
	v_lshlrev_b32_e32 v57, 16, v171
	v_pk_mul_f32 v[74:75], v[56:57], s[0:1] op_sel_hi:[1,0]
	v_lshlrev_b32_e32 v56, 16, v168
	v_and_b32_e32 v57, 0xffff0000, v168
	v_pk_mul_f32 v[76:77], v[56:57], s[0:1] op_sel_hi:[1,0]
	v_and_b32_e32 v56, 0xffff0000, v169
	v_lshlrev_b32_e32 v57, 16, v169
	v_pk_mul_f32 v[78:79], v[56:57], s[0:1] op_sel_hi:[1,0]
	v_or_b32_e32 v56, 2, v1
	v_readlane_b32 s0, v254, 48
	s_waitcnt vmcnt(1)
	v_or_b32_e32 v83, s6, v56
	v_or_b32_e32 v56, 4, v1
	v_readlane_b32 s1, v254, 49
	s_waitcnt vmcnt(0)
	v_or_b32_e32 v84, s6, v56
	v_or_b32_e32 v56, 6, v1
	v_lshl_add_u64 v[80:81], s[0:1], 1, v[156:157]
	v_or_b32_e32 v82, s6, v1
	v_or_b32_e32 v85, s6, v56
	v_mov_b32_e32 v86, v231
	v_mov_b32_e32 v87, v230
	v_readlane_b32 s0, v254, 29
	v_add_u32_e32 v133, 0xfffe8000, v86
	v_add_u32_e32 v134, 0xffff8000, v86
	s_mov_b32 s21, 0x80000000
.LBB0_724:
	s_add_i32 s8, s0, 8
	s_cmp_gt_i32 s8, s7
	s_cselect_b64 s[2:3], -1, 0
	s_and_b64 vcc, s[2:3], exec
	s_cselect_b32 s0, s0, s8
	s_lshl_b32 s0, s0, 4
	s_ashr_i32 s1, s0, 31
	s_lshl_b64 s[0:1], s[0:1], 7
	v_lshl_add_u64 v[60:61], v[80:81], 0, s[0:1]
	global_load_dwordx4 v[56:59], v[60:61], off
	s_nop 0
	global_load_dwordx4 v[60:63], v[60:61], off offset:1024
	s_waitcnt vmcnt(2)
	v_mfma_f32_16x16x32_bf16 v[100:103], v[28:31], v[44:47], 0
	v_mfma_f32_16x16x32_bf16 v[104:107], v[32:35], v[44:47], 0
	v_mfma_f32_16x16x32_bf16 v[108:111], v[24:27], v[44:47], 0
	v_mfma_f32_16x16x32_bf16 v[112:115], v[36:39], v[44:47], 0
	v_mfma_f32_16x16x32_bf16 v[100:103], v[20:23], v[40:43], v[100:103]
	v_mfma_f32_16x16x32_bf16 v[104:107], v[12:15], v[40:43], v[104:107]
	v_mfma_f32_16x16x32_bf16 v[108:111], v[16:19], v[40:43], v[108:111]
	v_mfma_f32_16x16x32_bf16 v[112:115], v[8:11], v[40:43], v[112:115]
	v_cmp_le_i32_e64 s[24:25], v87, v82
	v_cmp_le_i32_e64 s[26:27], v87, v83
	v_cmp_le_i32_e64 s[28:29], v87, v84
	v_cmp_le_i32_e64 s[30:31], v87, v85
	s_nop 0
	v_max_f32_e32 v100, 0, v100
	v_max_f32_e32 v101, 0, v101
	v_max_f32_e32 v102, 0, v102
	v_max_f32_e32 v103, 0, v103
	v_mul_f32_e32 v116, v65, v101
	v_fma_f32 v116, v64, v100, v116
	v_mul_f32_e32 v117, v67, v102
	v_add_f32_e32 v116, v117, v116
	v_fma_f32 v116, v66, v103, v116
	v_max_f32_e32 v104, 0, v104
	v_max_f32_e32 v105, 0, v105
	v_max_f32_e32 v106, 0, v106
	v_max_f32_e32 v107, 0, v107
	v_mul_f32_e32 v118, v69, v105
	v_fma_f32 v118, v68, v104, v118
	v_mul_f32_e32 v119, v71, v106
	v_add_f32_e32 v118, v119, v118
	v_fma_f32 v118, v70, v107, v118
	v_max_f32_e32 v108, 0, v108
	v_max_f32_e32 v109, 0, v109
	v_max_f32_e32 v110, 0, v110
	v_max_f32_e32 v111, 0, v111
	v_mul_f32_e32 v120, v73, v109
	v_fma_f32 v120, v72, v108, v120
	v_mul_f32_e32 v121, v75, v110
	v_add_f32_e32 v120, v121, v120
	v_fma_f32 v120, v74, v111, v120
	v_max_f32_e32 v112, 0, v112
	v_max_f32_e32 v113, 0, v113
	v_max_f32_e32 v114, 0, v114
	v_max_f32_e32 v115, 0, v115
	v_mul_f32_e32 v122, v77, v113
	v_fma_f32 v122, v76, v112, v122
	v_mul_f32_e32 v123, v79, v114
	v_add_f32_e32 v122, v123, v122
	v_fma_f32 v122, v78, v115, v122
	v_mov_b32_e32 v124, v116
	v_mov_b32_e32 v125, v118
	v_mov_b32_e32 v126, v120
	v_mov_b32_e32 v127, v122
	v_permlane16_swap_b32_e32 v116, v124
	v_permlane16_swap_b32_e32 v118, v125
	v_permlane16_swap_b32_e32 v120, v126
	v_permlane16_swap_b32_e32 v122, v127
	v_add_f32_e32 v116, v116, v124
	v_add_f32_e32 v118, v118, v125
	v_add_f32_e32 v120, v120, v126
	v_add_f32_e32 v122, v122, v127
	v_ashrrev_i32_e32 v124, 31, v116
	v_ashrrev_i32_e32 v125, 31, v118
	v_ashrrev_i32_e32 v126, 31, v120
	v_ashrrev_i32_e32 v127, 31, v122
	v_bitop3_b32 v116, v116, v124, s21 bitop3:0x1e
	v_bitop3_b32 v118, v118, v125, s21 bitop3:0x1e
	v_bitop3_b32 v120, v120, v126, s21 bitop3:0x1e
	v_bitop3_b32 v122, v122, v127, s21 bitop3:0x1e
	v_cndmask_b32_e64 v116, 0, v116, s[24:25]
	v_cndmask_b32_e64 v118, 0, v118, s[26:27]
	v_cndmask_b32_e64 v120, 0, v120, s[28:29]
	v_cndmask_b32_e64 v122, 0, v122, s[30:31]
	s_mov_b64 s[36:37], exec
	s_and_b64 exec, exec, s[10:11]
	ds_write_b32 v133, v116
	ds_write_b32 v133, v118 offset:32768
	ds_write_b32 v134, v120
	ds_write_b32 v134, v122 offset:32768
	s_mov_b64 exec, s[36:37]
	v_add_u32_e32 v133, 0x200, v133
	v_add_u32_e32 v134, 0x200, v134
	v_add_u32_e32 v87, 0x80, v87
	s_waitcnt vmcnt(0)
	v_mov_b64_e32 v[44:45], v[56:57]
	v_mov_b64_e32 v[46:47], v[58:59]
	v_mov_b64_e32 v[40:41], v[60:61]
	v_mov_b64_e32 v[42:43], v[62:63]
	s_mov_b32 s0, s8
	s_cbranch_vccz .LBB0_724
